# E2 conv: window-fill LDS reads issued in two batches into their own registers instead of a 25-deep read-wait-shift chain
# baseline (speedup 1.0000x reference)
; #define LAS __attribute__((address_space(3)))
; __device__ __forceinline__ unsigned pk2(float lo, float hi) { unsigned r; asm("v_cvt_pk_bf16_f32 %0, %1, %2" : "=v"(r) : "v"(lo), "v"(hi)); return r; }
; __device__ __forceinline__ float sigmoidf_(float x) { return __builtin_amdgcn_rcpf(1.0f + __builtin_amdgcn_exp2f(x * -1.44269504089f)); }
; __device__ __forceinline__ void phase_even_mix(CArgs a, LAS unsigned char* lds, int i2, int wv, int xw  ) {
;     ...
;         for (int it = 0; it < 8; ++it) { const int item = it * NTHR + tid, tt = item >> 6, cg = item & 63, p = t0 - 32 + tt;
;             u32x4 o = (u32x4){0u, 0u, 0u, 0u};
;             if (p >= 0) { const bf16* hp = HB + ((size_t)b * SEQ + p) * EVEN_IN + cg * 8; const u32x4 ra = *(const u32x4*)(hp + 512), rg = *(const u32x4*)(hp + 1024);
;                 o.x = pk2(bflo(ra.x) * sigmoidf_(bflo(rg.x)), bfhi(ra.x) * sigmoidf_(bfhi(rg.x))); o.y = pk2(bflo(ra.y) * sigmoidf_(bflo(rg.y)), bfhi(ra.y) * sigmoidf_(bfhi(rg.y)));
;                 o.z = pk2(bflo(ra.z) * sigmoidf_(bflo(rg.z)), bfhi(ra.z) * sigmoidf_(bfhi(rg.z))); o.w = pk2(bflo(ra.w) * sigmoidf_(bflo(rg.w)), bfhi(ra.w) * sigmoidf_(bfhi(rg.w))); }
;             *(LAS u32x4*)(glu + tt * 512 + cg * 8) = o; }
.Le2st_skip7:
	s_or_b64 exec, exec, s[16:17]
	s_waitcnt vmcnt(8)
	v_lshlrev_b32_e32 v1, 16, v232
	v_lshlrev_b32_e32 v10, 16, v236
	v_and_b32_e32 v236, 0xffff0000, v236
	v_lshlrev_b32_e32 v12, 16, v237
	v_and_b32_e32 v237, 0xffff0000, v237
	v_lshlrev_b32_e32 v14, 16, v238
	v_and_b32_e32 v238, 0xffff0000, v238
	v_lshlrev_b32_e32 v16, 16, v239
	v_and_b32_e32 v239, 0xffff0000, v239
	v_mul_f32_e32 v236, 0xbfb8aa3b, v236
	v_mul_f32_e32 v237, 0xbfb8aa3b, v237
	v_mul_f32_e32 v238, 0xbfb8aa3b, v238
	v_mul_f32_e32 v239, 0xbfb8aa3b, v239
	v_mul_f32_e32 v10, 0xbfb8aa3b, v10
	v_mul_f32_e32 v12, 0xbfb8aa3b, v12
	v_mul_f32_e32 v14, 0xbfb8aa3b, v14
	v_mul_f32_e32 v16, 0xbfb8aa3b, v16
	v_exp_f32_e32 v236, v236
	v_exp_f32_e32 v237, v237
	v_exp_f32_e32 v238, v238
	v_exp_f32_e32 v239, v239
	v_exp_f32_e32 v10, v10
	v_exp_f32_e32 v12, v12
	v_exp_f32_e32 v14, v14
	v_exp_f32_e32 v16, v16
	v_add_f32_e32 v236, 1.0, v236
	v_add_f32_e32 v237, 1.0, v237
	v_add_f32_e32 v238, 1.0, v238
	v_add_f32_e32 v239, 1.0, v239
	v_add_f32_e32 v10, 1.0, v10
	v_add_f32_e32 v12, 1.0, v12
	v_add_f32_e32 v14, 1.0, v14
	v_add_f32_e32 v16, 1.0, v16
	v_rcp_f32_e32 v236, v236
	v_rcp_f32_e32 v237, v237
	v_rcp_f32_e32 v238, v238
	v_rcp_f32_e32 v239, v239
	v_rcp_f32_e32 v10, v10
	v_rcp_f32_e32 v12, v12
	v_rcp_f32_e32 v14, v14
	v_rcp_f32_e32 v16, v16
	v_and_b32_e32 v232, 0xffff0000, v232
	v_lshlrev_b32_e32 v11, 16, v233
	v_and_b32_e32 v233, 0xffff0000, v233
	v_lshlrev_b32_e32 v13, 16, v234
	v_and_b32_e32 v234, 0xffff0000, v234
	v_lshlrev_b32_e32 v15, 16, v235
	v_and_b32_e32 v235, 0xffff0000, v235
	v_mul_f32_e32 v232, v236, v232
	v_mul_f32_e32 v233, v237, v233
	v_mul_f32_e32 v234, v238, v234
	v_mul_f32_e32 v235, v239, v235
	v_mul_f32_e32 v1, v10, v1
	v_mul_f32_e32 v236, v12, v11
	v_mul_f32_e32 v237, v14, v13
	v_mul_f32_e32 v238, v16, v15
	v_cvt_pk_bf16_f32 v232, v1, v232
	v_cvt_pk_bf16_f32 v233, v236, v233
	v_cvt_pk_bf16_f32 v234, v237, v234
	v_cvt_pk_bf16_f32 v235, v238, v235
	ds_write_b128 v149, v[232:235]
	s_waitcnt vmcnt(6)
	v_lshlrev_b32_e32 v1, 16, v240
	v_lshlrev_b32_e32 v10, 16, v244
	v_and_b32_e32 v244, 0xffff0000, v244
	v_lshlrev_b32_e32 v12, 16, v245
	v_and_b32_e32 v245, 0xffff0000, v245
	v_lshlrev_b32_e32 v14, 16, v246
	v_and_b32_e32 v246, 0xffff0000, v246
	v_lshlrev_b32_e32 v16, 16, v247
	v_and_b32_e32 v247, 0xffff0000, v247
	v_mul_f32_e32 v244, 0xbfb8aa3b, v244
	v_mul_f32_e32 v245, 0xbfb8aa3b, v245
	v_mul_f32_e32 v246, 0xbfb8aa3b, v246
	v_mul_f32_e32 v247, 0xbfb8aa3b, v247
	v_mul_f32_e32 v10, 0xbfb8aa3b, v10
	v_mul_f32_e32 v12, 0xbfb8aa3b, v12
	v_mul_f32_e32 v14, 0xbfb8aa3b, v14
	v_mul_f32_e32 v16, 0xbfb8aa3b, v16
	v_exp_f32_e32 v244, v244
	v_exp_f32_e32 v245, v245
	v_exp_f32_e32 v246, v246
	v_exp_f32_e32 v247, v247
	v_exp_f32_e32 v10, v10
	v_exp_f32_e32 v12, v12
	v_exp_f32_e32 v14, v14
	v_exp_f32_e32 v16, v16
	v_add_f32_e32 v244, 1.0, v244
	v_add_f32_e32 v245, 1.0, v245
	v_add_f32_e32 v246, 1.0, v246
	v_add_f32_e32 v247, 1.0, v247
	v_add_f32_e32 v10, 1.0, v10
	v_add_f32_e32 v12, 1.0, v12
	v_add_f32_e32 v14, 1.0, v14
	v_add_f32_e32 v16, 1.0, v16
	v_rcp_f32_e32 v244, v244
	v_rcp_f32_e32 v245, v245
	v_rcp_f32_e32 v246, v246
	v_rcp_f32_e32 v247, v247
	v_rcp_f32_e32 v10, v10
	v_rcp_f32_e32 v12, v12
	v_rcp_f32_e32 v14, v14
	v_rcp_f32_e32 v16, v16
	v_and_b32_e32 v240, 0xffff0000, v240
	v_lshlrev_b32_e32 v11, 16, v241
	v_and_b32_e32 v241, 0xffff0000, v241
	v_lshlrev_b32_e32 v13, 16, v242
	v_and_b32_e32 v242, 0xffff0000, v242
	v_lshlrev_b32_e32 v15, 16, v243
	v_and_b32_e32 v243, 0xffff0000, v243
	v_mul_f32_e32 v240, v244, v240
	v_mul_f32_e32 v241, v245, v241
	v_mul_f32_e32 v242, v246, v242
	v_mul_f32_e32 v243, v247, v243
	v_mul_f32_e32 v1, v10, v1
	v_mul_f32_e32 v244, v12, v11
	v_mul_f32_e32 v245, v14, v13
	v_mul_f32_e32 v246, v16, v15
	v_cvt_pk_bf16_f32 v240, v1, v240
	v_cvt_pk_bf16_f32 v241, v244, v241
	v_cvt_pk_bf16_f32 v242, v245, v242
	v_cvt_pk_bf16_f32 v243, v246, v243
	ds_write_b128 v150, v[240:243]
	s_waitcnt vmcnt(4)
	v_lshlrev_b32_e32 v1, 16, v208
	v_lshlrev_b32_e32 v10, 16, v212
	v_and_b32_e32 v212, 0xffff0000, v212
	v_lshlrev_b32_e32 v12, 16, v213
	v_and_b32_e32 v213, 0xffff0000, v213
	v_lshlrev_b32_e32 v14, 16, v214
	v_and_b32_e32 v214, 0xffff0000, v214
	v_lshlrev_b32_e32 v16, 16, v215
	v_and_b32_e32 v215, 0xffff0000, v215
	v_mul_f32_e32 v212, 0xbfb8aa3b, v212
	v_mul_f32_e32 v213, 0xbfb8aa3b, v213
	v_mul_f32_e32 v214, 0xbfb8aa3b, v214
	v_mul_f32_e32 v215, 0xbfb8aa3b, v215
	v_mul_f32_e32 v10, 0xbfb8aa3b, v10
	v_mul_f32_e32 v12, 0xbfb8aa3b, v12
	v_mul_f32_e32 v14, 0xbfb8aa3b, v14
	v_mul_f32_e32 v16, 0xbfb8aa3b, v16
	v_exp_f32_e32 v212, v212
	v_exp_f32_e32 v213, v213
	v_exp_f32_e32 v214, v214
	v_exp_f32_e32 v215, v215
	v_exp_f32_e32 v10, v10
	v_exp_f32_e32 v12, v12
	v_exp_f32_e32 v14, v14
	v_exp_f32_e32 v16, v16
	v_add_f32_e32 v212, 1.0, v212
	v_add_f32_e32 v213, 1.0, v213
	v_add_f32_e32 v214, 1.0, v214
	v_add_f32_e32 v215, 1.0, v215
	v_add_f32_e32 v10, 1.0, v10
	v_add_f32_e32 v12, 1.0, v12
	v_add_f32_e32 v14, 1.0, v14
	v_add_f32_e32 v16, 1.0, v16
	v_rcp_f32_e32 v212, v212
	v_rcp_f32_e32 v213, v213
	v_rcp_f32_e32 v214, v214
	v_rcp_f32_e32 v215, v215
	v_rcp_f32_e32 v10, v10
	v_rcp_f32_e32 v12, v12
	v_rcp_f32_e32 v14, v14
	v_rcp_f32_e32 v16, v16
	v_and_b32_e32 v208, 0xffff0000, v208
	v_lshlrev_b32_e32 v11, 16, v209
	v_and_b32_e32 v209, 0xffff0000, v209
	v_lshlrev_b32_e32 v13, 16, v210
	v_and_b32_e32 v210, 0xffff0000, v210
	v_lshlrev_b32_e32 v15, 16, v211
	v_and_b32_e32 v211, 0xffff0000, v211
	v_mul_f32_e32 v208, v212, v208
	v_mul_f32_e32 v209, v213, v209
	v_mul_f32_e32 v210, v214, v210
	v_mul_f32_e32 v211, v215, v211
	v_mul_f32_e32 v1, v10, v1
	v_mul_f32_e32 v212, v12, v11
	v_mul_f32_e32 v213, v14, v13
	v_mul_f32_e32 v214, v16, v15
	v_cvt_pk_bf16_f32 v208, v1, v208
	v_cvt_pk_bf16_f32 v209, v212, v209
	v_cvt_pk_bf16_f32 v210, v213, v210
	v_cvt_pk_bf16_f32 v211, v214, v211
	ds_write_b128 v151, v[208:211]
	s_waitcnt vmcnt(2)
; #define LAS __attribute__((address_space(3)))
; __device__ __forceinline__ unsigned pk2(float lo, float hi) { unsigned r; asm("v_cvt_pk_bf16_f32 %0, %1, %2" : "=v"(r) : "v"(lo), "v"(hi)); return r; }
; __device__ __forceinline__ float sigmoidf_(float x) { return __builtin_amdgcn_rcpf(1.0f + __builtin_amdgcn_exp2f(x * -1.44269504089f)); }
; __device__ __forceinline__ void phase_even_mix(CArgs a, LAS unsigned char* lds, int i2, int wv, int xw  ) {
;     ...
;         for (int it = 0; it < 8; ++it) { const int item = it * NTHR + tid, tt = item >> 6, cg = item & 63, p = t0 - 32 + tt;
;             u32x4 o = (u32x4){0u, 0u, 0u, 0u};
;             if (p >= 0) { const bf16* hp = HB + ((size_t)b * SEQ + p) * EVEN_IN + cg * 8; const u32x4 ra = *(const u32x4*)(hp + 512), rg = *(const u32x4*)(hp + 1024);
;                 o.x = pk2(bflo(ra.x) * sigmoidf_(bflo(rg.x)), bfhi(ra.x) * sigmoidf_(bfhi(rg.x))); o.y = pk2(bflo(ra.y) * sigmoidf_(bflo(rg.y)), bfhi(ra.y) * sigmoidf_(bfhi(rg.y)));
;                 o.z = pk2(bflo(ra.z) * sigmoidf_(bflo(rg.z)), bfhi(ra.z) * sigmoidf_(bfhi(rg.z))); o.w = pk2(bflo(ra.w) * sigmoidf_(bflo(rg.w)), bfhi(ra.w) * sigmoidf_(bfhi(rg.w))); }
;             *(LAS u32x4*)(glu + tt * 512 + cg * 8) = o; }
;         __syncthreads();
;         {
;             float w[31];
; #pragma unroll
;             for (int k = 0; k < 31; ++k) { unsigned off = (unsigned)c * 4u; asm volatile("" : "+v"(off)); w[k] = *(const float*)((const char*)(cw + k * 512) + off); }
	v_lshlrev_b32_e32 v1, 16, v216
	v_lshlrev_b32_e32 v10, 16, v220
	v_and_b32_e32 v220, 0xffff0000, v220
	v_lshlrev_b32_e32 v12, 16, v221
	v_and_b32_e32 v221, 0xffff0000, v221
	v_lshlrev_b32_e32 v14, 16, v222
	v_and_b32_e32 v222, 0xffff0000, v222
	v_lshlrev_b32_e32 v16, 16, v223
	v_and_b32_e32 v223, 0xffff0000, v223
	v_mul_f32_e32 v220, 0xbfb8aa3b, v220
	v_mul_f32_e32 v221, 0xbfb8aa3b, v221
	v_mul_f32_e32 v222, 0xbfb8aa3b, v222
	v_mul_f32_e32 v223, 0xbfb8aa3b, v223
	v_mul_f32_e32 v10, 0xbfb8aa3b, v10
	v_mul_f32_e32 v12, 0xbfb8aa3b, v12
	v_mul_f32_e32 v14, 0xbfb8aa3b, v14
	v_mul_f32_e32 v16, 0xbfb8aa3b, v16
	v_exp_f32_e32 v220, v220
	v_exp_f32_e32 v221, v221
	v_exp_f32_e32 v222, v222
	v_exp_f32_e32 v223, v223
	v_exp_f32_e32 v10, v10
	v_exp_f32_e32 v12, v12
	v_exp_f32_e32 v14, v14
	v_exp_f32_e32 v16, v16
	v_add_f32_e32 v220, 1.0, v220
	v_add_f32_e32 v221, 1.0, v221
	v_add_f32_e32 v222, 1.0, v222
	v_add_f32_e32 v223, 1.0, v223
	v_add_f32_e32 v10, 1.0, v10
	v_add_f32_e32 v12, 1.0, v12
	v_add_f32_e32 v14, 1.0, v14
	v_add_f32_e32 v16, 1.0, v16
	v_rcp_f32_e32 v220, v220
	v_rcp_f32_e32 v221, v221
	v_rcp_f32_e32 v222, v222
	v_rcp_f32_e32 v223, v223
	v_rcp_f32_e32 v10, v10
	v_rcp_f32_e32 v12, v12
	v_rcp_f32_e32 v14, v14
	v_rcp_f32_e32 v16, v16
	v_and_b32_e32 v216, 0xffff0000, v216
	v_lshlrev_b32_e32 v11, 16, v217
	v_and_b32_e32 v217, 0xffff0000, v217
	v_lshlrev_b32_e32 v13, 16, v218
	v_and_b32_e32 v218, 0xffff0000, v218
	v_lshlrev_b32_e32 v15, 16, v219
	v_and_b32_e32 v219, 0xffff0000, v219
	v_mul_f32_e32 v216, v220, v216
	v_mul_f32_e32 v217, v221, v217
	v_mul_f32_e32 v218, v222, v218
	v_mul_f32_e32 v219, v223, v219
	v_mul_f32_e32 v1, v10, v1
	v_mul_f32_e32 v220, v12, v11
	v_mul_f32_e32 v221, v14, v13
	v_mul_f32_e32 v222, v16, v15
	v_cvt_pk_bf16_f32 v216, v1, v216
	v_cvt_pk_bf16_f32 v217, v220, v217
	v_cvt_pk_bf16_f32 v218, v221, v218
	v_cvt_pk_bf16_f32 v219, v222, v219
	ds_write_b128 v141, v[216:219]
	s_waitcnt vmcnt(0)
	v_lshlrev_b32_e32 v1, 16, v224
	v_lshlrev_b32_e32 v10, 16, v228
	v_and_b32_e32 v228, 0xffff0000, v228
	v_lshlrev_b32_e32 v12, 16, v229
	v_and_b32_e32 v229, 0xffff0000, v229
	v_lshlrev_b32_e32 v14, 16, v230
	v_and_b32_e32 v230, 0xffff0000, v230
	v_lshlrev_b32_e32 v16, 16, v231
	v_and_b32_e32 v231, 0xffff0000, v231
	v_mul_f32_e32 v228, 0xbfb8aa3b, v228
	v_mul_f32_e32 v229, 0xbfb8aa3b, v229
	v_mul_f32_e32 v230, 0xbfb8aa3b, v230
	v_mul_f32_e32 v231, 0xbfb8aa3b, v231
	v_mul_f32_e32 v10, 0xbfb8aa3b, v10
	v_mul_f32_e32 v12, 0xbfb8aa3b, v12
	v_mul_f32_e32 v14, 0xbfb8aa3b, v14
	v_mul_f32_e32 v16, 0xbfb8aa3b, v16
	v_exp_f32_e32 v228, v228
	v_exp_f32_e32 v229, v229
	v_exp_f32_e32 v230, v230
	v_exp_f32_e32 v231, v231
	v_exp_f32_e32 v10, v10
	v_exp_f32_e32 v12, v12
	v_exp_f32_e32 v14, v14
	v_exp_f32_e32 v16, v16
	v_add_f32_e32 v228, 1.0, v228
	v_add_f32_e32 v229, 1.0, v229
	v_add_f32_e32 v230, 1.0, v230
	v_add_f32_e32 v231, 1.0, v231
	v_add_f32_e32 v10, 1.0, v10
	v_add_f32_e32 v12, 1.0, v12
	v_add_f32_e32 v14, 1.0, v14
	v_add_f32_e32 v16, 1.0, v16
	v_rcp_f32_e32 v228, v228
	v_rcp_f32_e32 v229, v229
	v_rcp_f32_e32 v230, v230
	v_rcp_f32_e32 v231, v231
	v_rcp_f32_e32 v10, v10
	v_rcp_f32_e32 v12, v12
	v_rcp_f32_e32 v14, v14
	v_rcp_f32_e32 v16, v16
	v_and_b32_e32 v224, 0xffff0000, v224
	v_lshlrev_b32_e32 v11, 16, v225
	v_and_b32_e32 v225, 0xffff0000, v225
	v_lshlrev_b32_e32 v13, 16, v226
	v_and_b32_e32 v226, 0xffff0000, v226
	v_lshlrev_b32_e32 v15, 16, v227
	v_and_b32_e32 v227, 0xffff0000, v227
	v_mul_f32_e32 v224, v228, v224
	v_mul_f32_e32 v225, v229, v225
	v_mul_f32_e32 v226, v230, v226
	v_mul_f32_e32 v227, v231, v227
	v_mul_f32_e32 v1, v10, v1
	v_mul_f32_e32 v228, v12, v11
	v_mul_f32_e32 v229, v14, v13
	v_mul_f32_e32 v230, v16, v15
	v_cvt_pk_bf16_f32 v224, v1, v224
	v_cvt_pk_bf16_f32 v225, v228, v225
	v_cvt_pk_bf16_f32 v226, v229, v226
	v_cvt_pk_bf16_f32 v227, v230, v227
	ds_write_b128 v142, v[224:227]
	v_mov_b32_e32 v0, v29
	s_waitcnt vmcnt(0) lgkmcnt(0)
	s_barrier
	v_mov_b32_e32 v1, v29
	global_load_dword v0, v0, s[90:91]
	v_mov_b32_e32 v2, v29
	v_readlane_b32 s16, v254, 33
	global_load_dword v1, v1, s[90:91] offset:2048
	v_readlane_b32 s17, v254, 34
	v_mov_b32_e32 v3, v29
	v_mov_b32_e32 v4, v29
	v_mov_b32_e32 v5, v29
	v_mov_b32_e32 v6, v29
	v_mov_b32_e32 v7, v29
	global_load_dword v2, v2, s[16:17]
	v_readlane_b32 s16, v254, 35
	v_readlane_b32 s17, v254, 36
	v_mov_b32_e32 v8, v29
	v_mov_b32_e32 v9, v29
	v_mov_b32_e32 v10, v29
	v_mov_b32_e32 v11, v29
	v_mov_b32_e32 v12, v29
	global_load_dword v3, v3, s[16:17]
	v_readlane_b32 s16, v254, 37
	v_readlane_b32 s17, v254, 38
	v_mov_b32_e32 v13, v29
	v_mov_b32_e32 v14, v29
	v_mov_b32_e32 v15, v29
	v_mov_b32_e32 v16, v29
	v_mov_b32_e32 v17, v29
	global_load_dword v4, v4, s[16:17]
	v_readlane_b32 s16, v254, 39
	v_readlane_b32 s17, v254, 40
	v_mov_b32_e32 v18, v29
	v_mov_b32_e32 v19, v29
	v_mov_b32_e32 v20, v29
	v_mov_b32_e32 v21, v29
	v_mov_b32_e32 v22, v29
	global_load_dword v5, v5, s[16:17]
	v_readlane_b32 s16, v254, 41
	v_readlane_b32 s17, v254, 42
	v_mov_b32_e32 v23, v29
	v_mov_b32_e32 v152, v29
	v_mov_b32_e32 v154, v29
	v_mov_b32_e32 v155, v29
	v_mov_b32_e32 v156, v29
	global_load_dword v6, v6, s[16:17]
	v_readlane_b32 s16, v254, 43
	v_readlane_b32 s17, v254, 44
	v_mov_b32_e32 v157, v29
	v_mov_b32_e32 v158, v29
	v_mov_b32_e32 v159, v29
	s_add_i32 s19, s15, -16
	s_nop 0
	global_load_dword v7, v7, s[16:17]
	v_readlane_b32 s16, v254, 45
	v_readlane_b32 s17, v254, 46
	s_nop 4
	global_load_dword v8, v8, s[16:17]
	v_readlane_b32 s16, v254, 47
	v_readlane_b32 s17, v254, 48
	s_nop 4
	global_load_dword v9, v9, s[16:17]
	v_readlane_b32 s16, v254, 49
	v_readlane_b32 s17, v254, 50
	s_nop 4
	global_load_dword v10, v10, s[16:17]
; __device__ __forceinline__ void phase_even_mix(CArgs a, LAS unsigned char* lds, int i2, int wv, int xw  ) {
;     ...
;             const float cb = a->in[I_CONVB][i2 * 512 + c];
;             float win[34];
; #pragma clang loop unroll(full)
;             for (int r = 0; r < 64; ++r) {
;                 win[r % 34] = bf2f(glu[r * 512 + c]);
;                 if (r >= 32) { float y = cb;
; #pragma unroll
;                     for (int k = 0; k < 31; ++k) y += w[k] * win[(r - 30 + k) % 34];
;                     ybuf[(r - 32) * 512 + c] = y; }
	v_readlane_b32 s16, v254, 51
	v_readlane_b32 s17, v254, 52
	s_nop 4
	global_load_dword v11, v11, s[16:17]
	v_readlane_b32 s16, v254, 53
	v_readlane_b32 s17, v254, 54
	s_nop 4
	global_load_dword v12, v12, s[16:17]
	v_readlane_b32 s16, v254, 55
	v_readlane_b32 s17, v254, 56
	s_nop 4
	global_load_dword v13, v13, s[16:17]
	v_readlane_b32 s16, v254, 57
	v_readlane_b32 s17, v254, 58
	s_nop 4
	global_load_dword v14, v14, s[16:17]
	v_readlane_b32 s16, v254, 59
	v_readlane_b32 s17, v254, 60
	s_nop 4
	global_load_dword v15, v15, s[16:17]
	v_readlane_b32 s16, v254, 61
	v_readlane_b32 s17, v254, 62
	s_nop 4
	global_load_dword v16, v16, s[16:17]
	v_readlane_b32 s16, v254, 63
	v_readlane_b32 s17, v255, 0
	s_nop 4
	global_load_dword v17, v17, s[16:17]
	v_readlane_b32 s16, v255, 1
	v_readlane_b32 s17, v255, 2
	s_nop 4
	global_load_dword v18, v18, s[16:17]
	global_load_dword v19, v19, s[40:41]
	global_load_dword v20, v20, s[84:85]
	global_load_dword v21, v21, s[26:27]
	global_load_dword v22, v22, s[20:21]
	global_load_dword v23, v23, s[4:5]
	global_load_dword v152, v152, s[2:3]
	global_load_dword v154, v154, s[24:25]
	global_load_dword v155, v155, s[30:31]
	global_load_dword v156, v156, s[0:1]
	global_load_dword v157, v157, s[72:73]
	global_load_dword v158, v158, s[74:75]
	s_load_dwordx2 s[16:17], s[88:89], 0x38
	ds_read_u16 v162, v35 offset:3072
	ds_read_u16 v163, v35 offset:4096
	ds_read_u16 v164, v35 offset:5120
	ds_read_u16 v165, v35 offset:6144
	ds_read_u16 v166, v35 offset:7168
	s_waitcnt lgkmcnt(0)
	v_lshl_add_u64 v[160:161], v[26:27], 2, s[16:17]
	global_load_dword v160, v[160:161], off
	ds_read_u16 v161, v35 offset:2048
	global_load_dword v159, v159, s[76:77]
	v_lshlrev_b32_e32 v167, 16, v166
	ds_read_u16 v174, v35 offset:8192
	ds_read_u16 v176, v35 offset:9216
	ds_read_u16 v177, v35 offset:10240
	ds_read_u16 v192, v35 offset:11264
	ds_read_u16 v193, v35 offset:12288
	ds_read_u16 v194, v35 offset:13312
	ds_read_u16 v196, v35 offset:14336
	ds_read_u16 v198, v35 offset:15360
	ds_read_u16 v205, v35 offset:16384
	ds_read_u16 v204, v35 offset:17408
	ds_read_u16 v203, v35 offset:18432
	ds_read_u16 v202, v35 offset:19456
	ds_read_u16 v201, v35 offset:20480
	s_waitcnt lgkmcnt(0)
	ds_read_u16 v200, v35 offset:21504
	ds_read_u16 v199, v35 offset:22528
	ds_read_u16 v197, v35 offset:23552
	ds_read_u16 v195, v35 offset:24576
	ds_read_u16 v175, v35 offset:25600
	ds_read_u16 v173, v35 offset:26624
	ds_read_u16 v172, v35 offset:27648
	ds_read_u16 v171, v35 offset:28672
	ds_read_u16 v170, v35 offset:29696
	ds_read_u16 v169, v35 offset:30720
	ds_read_u16 v168, v35 offset:31744
	ds_read_u16 v166, v35 offset:32768
	v_lshlrev_b32_e32 v174, 16, v174
	v_lshlrev_b32_e32 v176, 16, v176
	v_lshlrev_b32_e32 v177, 16, v177
	v_lshlrev_b32_e32 v192, 16, v192
	v_lshlrev_b32_e32 v193, 16, v193
	v_lshlrev_b32_e32 v194, 16, v194
	v_lshlrev_b32_e32 v196, 16, v196
	v_lshlrev_b32_e32 v198, 16, v198
	v_lshlrev_b32_e32 v205, 16, v205
	v_lshlrev_b32_e32 v204, 16, v204
	v_lshlrev_b32_e32 v203, 16, v203
	v_lshlrev_b32_e32 v202, 16, v202
	v_lshlrev_b32_e32 v201, 16, v201
	s_waitcnt lgkmcnt(0)
	v_lshlrev_b32_e32 v200, 16, v200
	v_lshlrev_b32_e32 v199, 16, v199
	v_lshlrev_b32_e32 v197, 16, v197
	v_lshlrev_b32_e32 v195, 16, v195
	v_lshlrev_b32_e32 v175, 16, v175
	v_lshlrev_b32_e32 v173, 16, v173
	v_lshlrev_b32_e32 v172, 16, v172
	v_lshlrev_b32_e32 v171, 16, v171
	v_lshlrev_b32_e32 v170, 16, v170
	v_lshlrev_b32_e32 v169, 16, v169
	v_lshlrev_b32_e32 v168, 16, v168
	v_lshlrev_b32_e32 v162, 16, v162
	v_lshlrev_b32_e32 v163, 16, v163
	v_lshlrev_b32_e32 v164, 16, v164
	v_lshlrev_b32_e32 v165, 16, v165
	s_waitcnt vmcnt(1)
	v_fma_f32 v178, v0, v192, v160
	v_fmac_f32_e32 v178, v1, v193
	v_fmac_f32_e32 v178, v2, v194
	v_fmac_f32_e32 v178, v3, v196
	v_fmac_f32_e32 v178, v4, v198
	v_fmac_f32_e32 v178, v5, v205
	v_fmac_f32_e32 v178, v6, v204
	v_fmac_f32_e32 v178, v7, v203
	v_fmac_f32_e32 v178, v8, v202
	v_fmac_f32_e32 v178, v9, v201
	v_fmac_f32_e32 v178, v10, v200
	v_fmac_f32_e32 v178, v11, v199
	v_fmac_f32_e32 v178, v12, v197
	v_fmac_f32_e32 v178, v13, v195
	v_fmac_f32_e32 v178, v14, v175
	v_fmac_f32_e32 v178, v15, v173
	v_fmac_f32_e32 v178, v16, v172
	v_fmac_f32_e32 v178, v17, v171
	v_fmac_f32_e32 v178, v18, v170
	v_fmac_f32_e32 v178, v19, v169
	v_lshlrev_b32_e32 v161, 16, v161
	v_fma_f32 v161, v0, v161, v160
	v_fmac_f32_e32 v161, v1, v162
	v_fmac_f32_e32 v161, v2, v163
	v_fmac_f32_e32 v161, v3, v164
	v_fmac_f32_e32 v161, v4, v165
	v_fmac_f32_e32 v161, v5, v167
	v_fmac_f32_e32 v161, v6, v174
	v_fmac_f32_e32 v161, v7, v176
	v_fma_f32 v162, v0, v162, v160
	v_fmac_f32_e32 v161, v8, v177
	v_fmac_f32_e32 v162, v1, v163
	v_fmac_f32_e32 v161, v9, v192
	v_fmac_f32_e32 v162, v2, v164
	v_fmac_f32_e32 v161, v10, v193
	v_fmac_f32_e32 v162, v3, v165
	v_fmac_f32_e32 v161, v11, v194
	v_fmac_f32_e32 v162, v4, v167
	v_fmac_f32_e32 v161, v12, v196
	v_fmac_f32_e32 v162, v5, v174
	v_fmac_f32_e32 v161, v13, v198
	v_fmac_f32_e32 v162, v6, v176
	v_fmac_f32_e32 v161, v14, v205
	v_fmac_f32_e32 v162, v7, v177
	v_fma_f32 v163, v0, v163, v160
	v_fmac_f32_e32 v161, v15, v204
	v_fmac_f32_e32 v162, v8, v192
	v_fmac_f32_e32 v163, v1, v164
	v_fmac_f32_e32 v161, v16, v203
	v_fmac_f32_e32 v162, v9, v193
	v_fmac_f32_e32 v163, v2, v165
	v_fmac_f32_e32 v161, v17, v202
	v_fmac_f32_e32 v162, v10, v194
	v_fmac_f32_e32 v163, v3, v167
	v_fmac_f32_e32 v161, v18, v201
	v_fmac_f32_e32 v162, v11, v196
	v_fmac_f32_e32 v163, v4, v174
	v_fmac_f32_e32 v161, v19, v200
	v_fmac_f32_e32 v162, v12, v198
	v_fmac_f32_e32 v163, v5, v176
	v_fmac_f32_e32 v161, v20, v199
	v_fmac_f32_e32 v162, v13, v205
	v_fmac_f32_e32 v163, v6, v177
	v_fmac_f32_e32 v161, v21, v197
	v_fmac_f32_e32 v162, v14, v204
	v_fmac_f32_e32 v163, v7, v192
	v_fma_f32 v164, v0, v164, v160
	v_fmac_f32_e32 v161, v22, v195
	v_fmac_f32_e32 v162, v15, v203
	v_fmac_f32_e32 v163, v8, v193
	v_fmac_f32_e32 v164, v1, v165
	v_fmac_f32_e32 v161, v23, v175
	v_fmac_f32_e32 v162, v16, v202
	v_fmac_f32_e32 v163, v9, v194
	v_fmac_f32_e32 v164, v2, v167
	v_fmac_f32_e32 v161, v152, v173
	v_fmac_f32_e32 v162, v17, v201
	v_fmac_f32_e32 v163, v10, v196
	v_fmac_f32_e32 v164, v3, v174
	v_fmac_f32_e32 v161, v154, v172
	v_fmac_f32_e32 v162, v18, v200
	v_fmac_f32_e32 v163, v11, v198
	v_fmac_f32_e32 v164, v4, v176
	v_fmac_f32_e32 v161, v155, v171
	v_fmac_f32_e32 v162, v19, v199
	v_fmac_f32_e32 v163, v12, v205
	v_fmac_f32_e32 v164, v5, v177
	v_fmac_f32_e32 v161, v156, v170
	v_fmac_f32_e32 v162, v20, v197
	v_fmac_f32_e32 v163, v13, v204
	v_fmac_f32_e32 v164, v6, v192
	v_fmac_f32_e32 v161, v157, v169
	v_fmac_f32_e32 v162, v21, v195
	v_fmac_f32_e32 v163, v14, v203
	v_fmac_f32_e32 v164, v7, v193
	v_fma_f32 v165, v0, v165, v160
	s_waitcnt lgkmcnt(0)
; __device__ __forceinline__ void phase_even_mix(CArgs a, LAS unsigned char* lds, int i2, int wv, int xw  ) {
;     ...
;             for (int r = 0; r < 64; ++r) {
;                 win[r % 34] = bf2f(glu[r * 512 + c]);
;                 if (r >= 32) { float y = cb;
; #pragma unroll
;                     for (int k = 0; k < 31; ++k) y += w[k] * win[(r - 30 + k) % 34];
;                     ybuf[(r - 32) * 512 + c] = y; }
	v_lshlrev_b32_e32 v166, 16, v166
	v_fmac_f32_e32 v161, v158, v168
	v_fmac_f32_e32 v162, v22, v175
	v_fmac_f32_e32 v163, v15, v202
	v_fmac_f32_e32 v164, v8, v194
	v_fmac_f32_e32 v165, v1, v167
	s_waitcnt vmcnt(0)
	v_fmac_f32_e32 v161, v159, v166
	v_fmac_f32_e32 v162, v23, v173
	v_fmac_f32_e32 v163, v16, v201
	v_fmac_f32_e32 v164, v9, v196
	v_fmac_f32_e32 v165, v2, v174
	ds_write_b32 v78, v161
	ds_read_u16 v161, v35 offset:33792
	v_fmac_f32_e32 v162, v152, v172
	v_fmac_f32_e32 v163, v17, v200
	v_fmac_f32_e32 v164, v10, v198
	v_fmac_f32_e32 v165, v3, v176
	v_fmac_f32_e32 v162, v154, v171
	v_fmac_f32_e32 v163, v18, v199
	v_fmac_f32_e32 v164, v11, v205
	v_fmac_f32_e32 v165, v4, v177
	v_fmac_f32_e32 v162, v155, v170
	v_fmac_f32_e32 v163, v19, v197
	v_fmac_f32_e32 v164, v12, v204
	v_fmac_f32_e32 v165, v5, v192
	v_fmac_f32_e32 v162, v156, v169
	v_fmac_f32_e32 v163, v20, v195
	v_fmac_f32_e32 v164, v13, v203
	v_fmac_f32_e32 v165, v6, v193
	v_fmac_f32_e32 v162, v157, v168
	v_fmac_f32_e32 v163, v21, v175
	v_fmac_f32_e32 v164, v14, v202
	v_fmac_f32_e32 v165, v7, v194
	v_fma_f32 v167, v0, v167, v160
	s_waitcnt lgkmcnt(0)
	v_lshlrev_b32_e32 v161, 16, v161
	v_fmac_f32_e32 v162, v158, v166
	v_fmac_f32_e32 v163, v22, v173
	v_fmac_f32_e32 v164, v15, v201
	v_fmac_f32_e32 v165, v8, v196
	v_fmac_f32_e32 v167, v1, v174
	v_fmac_f32_e32 v162, v159, v161
	v_fmac_f32_e32 v163, v23, v172
	v_fmac_f32_e32 v164, v16, v200
	v_fmac_f32_e32 v165, v9, v198
	v_fmac_f32_e32 v167, v2, v176
	ds_write_b32 v79, v162
	ds_read_u16 v162, v35 offset:34816
	v_fmac_f32_e32 v163, v152, v171
	v_fmac_f32_e32 v164, v17, v199
	v_fmac_f32_e32 v165, v10, v205
	v_fmac_f32_e32 v167, v3, v177
	v_fmac_f32_e32 v163, v154, v170
	v_fmac_f32_e32 v164, v18, v197
	v_fmac_f32_e32 v165, v11, v204
	v_fmac_f32_e32 v167, v4, v192
	v_fmac_f32_e32 v163, v155, v169
	v_fmac_f32_e32 v164, v19, v195
	v_fmac_f32_e32 v165, v12, v203
	v_fmac_f32_e32 v167, v5, v193
	v_fmac_f32_e32 v163, v156, v168
	v_fmac_f32_e32 v164, v20, v175
	v_fmac_f32_e32 v165, v13, v202
	v_fmac_f32_e32 v167, v6, v194
	v_fmac_f32_e32 v163, v157, v166
	v_fmac_f32_e32 v164, v21, v173
	v_fmac_f32_e32 v165, v14, v201
	v_fmac_f32_e32 v167, v7, v196
	v_fma_f32 v174, v0, v174, v160
	s_waitcnt lgkmcnt(0)
	v_lshlrev_b32_e32 v162, 16, v162
	v_fmac_f32_e32 v163, v158, v161
	v_fmac_f32_e32 v164, v22, v172
	v_fmac_f32_e32 v165, v15, v200
	v_fmac_f32_e32 v167, v8, v198
	v_fmac_f32_e32 v174, v1, v176
	v_fmac_f32_e32 v163, v159, v162
	v_fmac_f32_e32 v164, v23, v171
	v_fmac_f32_e32 v165, v16, v199
	v_fmac_f32_e32 v167, v9, v205
	v_fmac_f32_e32 v174, v2, v177
	ds_write_b32 v80, v163
	ds_read_u16 v163, v35 offset:35840
	v_fmac_f32_e32 v164, v152, v170
	v_fmac_f32_e32 v165, v17, v197
	v_fmac_f32_e32 v167, v10, v204
	v_fmac_f32_e32 v174, v3, v192
	v_fmac_f32_e32 v164, v154, v169
	v_fmac_f32_e32 v165, v18, v195
	v_fmac_f32_e32 v167, v11, v203
	v_fmac_f32_e32 v174, v4, v193
	v_fmac_f32_e32 v164, v155, v168
	v_fmac_f32_e32 v165, v19, v175
	v_fmac_f32_e32 v167, v12, v202
	v_fmac_f32_e32 v174, v5, v194
	v_fmac_f32_e32 v164, v156, v166
	v_fmac_f32_e32 v165, v20, v173
	v_fmac_f32_e32 v167, v13, v201
	v_fmac_f32_e32 v174, v6, v196
	v_fmac_f32_e32 v164, v157, v161
	v_fmac_f32_e32 v165, v21, v172
	v_fmac_f32_e32 v167, v14, v200
	v_fmac_f32_e32 v174, v7, v198
	v_fma_f32 v176, v0, v176, v160
	s_waitcnt lgkmcnt(0)
	v_lshlrev_b32_e32 v163, 16, v163
	v_fmac_f32_e32 v164, v158, v162
	v_fmac_f32_e32 v165, v22, v171
	v_fmac_f32_e32 v167, v15, v199
	v_fmac_f32_e32 v174, v8, v205
	v_fmac_f32_e32 v176, v1, v177
	v_fmac_f32_e32 v164, v159, v163
	v_fmac_f32_e32 v165, v23, v170
	v_fmac_f32_e32 v167, v16, v197
	v_fmac_f32_e32 v174, v9, v204
	v_fmac_f32_e32 v176, v2, v192
	ds_write_b32 v81, v164
	ds_read_u16 v164, v35 offset:36864
	v_fmac_f32_e32 v165, v152, v169
	v_fmac_f32_e32 v167, v17, v195
	v_fmac_f32_e32 v174, v10, v203
	v_fmac_f32_e32 v176, v3, v193
	v_fmac_f32_e32 v165, v154, v168
	v_fmac_f32_e32 v167, v18, v175
	v_fmac_f32_e32 v174, v11, v202
	v_fmac_f32_e32 v176, v4, v194
	v_fmac_f32_e32 v165, v155, v166
	v_fmac_f32_e32 v167, v19, v173
	v_fmac_f32_e32 v174, v12, v201
	v_fmac_f32_e32 v176, v5, v196
	v_fmac_f32_e32 v165, v156, v161
	v_fmac_f32_e32 v167, v20, v172
	v_fmac_f32_e32 v174, v13, v200
	v_fmac_f32_e32 v176, v6, v198
	v_fmac_f32_e32 v165, v157, v162
	v_fmac_f32_e32 v167, v21, v171
	v_fmac_f32_e32 v174, v14, v199
	v_fmac_f32_e32 v176, v7, v205
	v_fma_f32 v177, v0, v177, v160
	s_waitcnt lgkmcnt(0)
	v_lshlrev_b32_e32 v164, 16, v164
	v_fmac_f32_e32 v165, v158, v163
	v_fmac_f32_e32 v167, v22, v170
	v_fmac_f32_e32 v174, v15, v197
	v_fmac_f32_e32 v176, v8, v204
	v_fmac_f32_e32 v177, v1, v192
	v_fmac_f32_e32 v165, v159, v164
	v_fmac_f32_e32 v167, v23, v169
	v_fmac_f32_e32 v174, v16, v195
	v_fmac_f32_e32 v176, v9, v203
	v_fmac_f32_e32 v177, v2, v193
	ds_write_b32 v82, v165
	ds_read_u16 v165, v35 offset:37888
	v_fmac_f32_e32 v167, v152, v168
	v_fmac_f32_e32 v174, v17, v175
	v_fmac_f32_e32 v176, v10, v202
	v_fmac_f32_e32 v177, v3, v194
	v_fmac_f32_e32 v167, v154, v166
	v_fmac_f32_e32 v174, v18, v173
	v_fmac_f32_e32 v176, v11, v201
	v_fmac_f32_e32 v177, v4, v196
	v_fmac_f32_e32 v167, v155, v161
	v_fmac_f32_e32 v174, v19, v172
	v_fmac_f32_e32 v176, v12, v200
	v_fmac_f32_e32 v177, v5, v198
	v_fmac_f32_e32 v167, v156, v162
	v_fmac_f32_e32 v174, v20, v171
	v_fmac_f32_e32 v176, v13, v199
	v_fmac_f32_e32 v177, v6, v205
	v_fmac_f32_e32 v167, v157, v163
	v_fmac_f32_e32 v174, v21, v170
	v_fmac_f32_e32 v176, v14, v197
	v_fmac_f32_e32 v177, v7, v204
	s_waitcnt lgkmcnt(0)
; __device__ __forceinline__ void phase_even_mix(CArgs a, LAS unsigned char* lds, int i2, int wv, int xw  ) {
;     ...
;             for (int r = 0; r < 64; ++r) {
;                 win[r % 34] = bf2f(glu[r * 512 + c]);
;                 if (r >= 32) { float y = cb;
; #pragma unroll
;                     for (int k = 0; k < 31; ++k) y += w[k] * win[(r - 30 + k) % 34];
;                     ybuf[(r - 32) * 512 + c] = y; }
	v_lshlrev_b32_e32 v165, 16, v165
	v_fmac_f32_e32 v167, v158, v164
	v_fmac_f32_e32 v174, v22, v169
	v_fmac_f32_e32 v176, v15, v195
	v_fmac_f32_e32 v177, v8, v203
	v_fmac_f32_e32 v167, v159, v165
	v_fmac_f32_e32 v174, v23, v168
	v_fmac_f32_e32 v176, v16, v175
	v_fmac_f32_e32 v177, v9, v202
	ds_write_b32 v83, v167
	ds_read_u16 v167, v35 offset:38912
	v_fmac_f32_e32 v174, v152, v166
	v_fmac_f32_e32 v176, v17, v173
	v_fmac_f32_e32 v177, v10, v201
	v_fmac_f32_e32 v174, v154, v161
	v_fmac_f32_e32 v176, v18, v172
	v_fmac_f32_e32 v177, v11, v200
	v_fmac_f32_e32 v174, v155, v162
	v_fmac_f32_e32 v176, v19, v171
	v_fmac_f32_e32 v177, v12, v199
	v_fmac_f32_e32 v174, v156, v163
	v_fmac_f32_e32 v176, v20, v170
	v_fmac_f32_e32 v177, v13, v197
	v_fmac_f32_e32 v174, v157, v164
	v_fmac_f32_e32 v176, v21, v169
	v_fmac_f32_e32 v177, v14, v195
	s_waitcnt lgkmcnt(0)
	v_lshlrev_b32_e32 v167, 16, v167
	v_fmac_f32_e32 v174, v158, v165
	v_fmac_f32_e32 v176, v22, v168
	v_fmac_f32_e32 v177, v15, v175
	v_fmac_f32_e32 v174, v159, v167
	v_fmac_f32_e32 v176, v23, v166
	v_fmac_f32_e32 v177, v16, v173
	ds_write_b32 v84, v174
	ds_read_u16 v174, v35 offset:39936
	v_fmac_f32_e32 v176, v152, v161
	v_fmac_f32_e32 v177, v17, v172
	v_fmac_f32_e32 v176, v154, v162
	v_fmac_f32_e32 v177, v18, v171
	v_fmac_f32_e32 v176, v155, v163
	v_fmac_f32_e32 v177, v19, v170
	v_fmac_f32_e32 v176, v156, v164
	v_fmac_f32_e32 v177, v20, v169
	v_fmac_f32_e32 v176, v157, v165
	v_fmac_f32_e32 v177, v21, v168
	s_waitcnt lgkmcnt(0)
	v_lshlrev_b32_e32 v174, 16, v174
	v_fmac_f32_e32 v176, v158, v167
	v_fmac_f32_e32 v177, v22, v166
	v_fmac_f32_e32 v176, v159, v174
	v_fmac_f32_e32 v177, v23, v161
	ds_write_b32 v85, v176
	ds_read_u16 v176, v35 offset:40960
	v_fmac_f32_e32 v177, v152, v162
	v_fmac_f32_e32 v177, v154, v163
	v_fmac_f32_e32 v177, v155, v164
	v_fmac_f32_e32 v177, v156, v165
	v_fmac_f32_e32 v178, v20, v168
	v_fmac_f32_e32 v177, v157, v167
	v_fmac_f32_e32 v178, v21, v166
	s_waitcnt lgkmcnt(0)
	v_lshlrev_b32_e32 v176, 16, v176
	v_fmac_f32_e32 v177, v158, v174
	v_fmac_f32_e32 v178, v22, v161
	v_fmac_f32_e32 v177, v159, v176
	v_fmac_f32_e32 v178, v23, v162
	ds_write_b32 v86, v177
	ds_read_u16 v177, v35 offset:41984
	v_fmac_f32_e32 v178, v152, v163
	v_fmac_f32_e32 v178, v154, v164
	v_fmac_f32_e32 v178, v155, v165
	v_fmac_f32_e32 v178, v156, v167
	v_fmac_f32_e32 v178, v157, v174
	s_waitcnt lgkmcnt(0)
	v_lshlrev_b32_e32 v177, 16, v177
	v_fmac_f32_e32 v178, v158, v176
	v_fmac_f32_e32 v178, v159, v177
	ds_write_b32 v87, v178
	ds_read_u16 v178, v35 offset:43008
	s_waitcnt lgkmcnt(0)
	v_lshlrev_b32_e32 v192, 16, v178
	v_fma_f32 v178, v0, v193, v160
	v_fmac_f32_e32 v178, v1, v194
	v_fmac_f32_e32 v178, v2, v196
	v_fmac_f32_e32 v178, v3, v198
	v_fmac_f32_e32 v178, v4, v205
	v_fmac_f32_e32 v178, v5, v204
	v_fmac_f32_e32 v178, v6, v203
	v_fmac_f32_e32 v178, v7, v202
	v_fmac_f32_e32 v178, v8, v201
	v_fmac_f32_e32 v178, v9, v200
	v_fmac_f32_e32 v178, v10, v199
	v_fmac_f32_e32 v178, v11, v197
	v_fmac_f32_e32 v178, v12, v195
	v_fmac_f32_e32 v178, v13, v175
	v_fmac_f32_e32 v178, v14, v173
	v_fmac_f32_e32 v178, v15, v172
	v_fmac_f32_e32 v178, v16, v171
	v_fmac_f32_e32 v178, v17, v170
	v_fmac_f32_e32 v178, v18, v169
	v_fmac_f32_e32 v178, v19, v168
	v_fmac_f32_e32 v178, v20, v166
	v_fmac_f32_e32 v178, v21, v161
	v_fmac_f32_e32 v178, v22, v162
	v_fmac_f32_e32 v178, v23, v163
	v_fmac_f32_e32 v178, v152, v164
	v_fmac_f32_e32 v178, v154, v165
	v_fmac_f32_e32 v178, v155, v167
	v_fmac_f32_e32 v178, v156, v174
	v_fmac_f32_e32 v178, v157, v176
	v_fmac_f32_e32 v178, v158, v177
	v_fmac_f32_e32 v178, v159, v192
	ds_write_b32 v88, v178
	ds_read_u16 v178, v35 offset:44032
	s_waitcnt lgkmcnt(0)
	v_lshlrev_b32_e32 v193, 16, v178
	v_fma_f32 v178, v0, v194, v160
	v_fmac_f32_e32 v178, v1, v196
	v_fmac_f32_e32 v178, v2, v198
	v_fmac_f32_e32 v178, v3, v205
	v_fmac_f32_e32 v178, v4, v204
	v_fmac_f32_e32 v178, v5, v203
	v_fmac_f32_e32 v178, v6, v202
	v_fmac_f32_e32 v178, v7, v201
	v_fmac_f32_e32 v178, v8, v200
	v_fmac_f32_e32 v178, v9, v199
	v_fmac_f32_e32 v178, v10, v197
	v_fmac_f32_e32 v178, v11, v195
	v_fmac_f32_e32 v178, v12, v175
	v_fmac_f32_e32 v178, v13, v173
	v_fmac_f32_e32 v178, v14, v172
	v_fmac_f32_e32 v178, v15, v171
	v_fmac_f32_e32 v178, v16, v170
	v_fmac_f32_e32 v178, v17, v169
	v_fmac_f32_e32 v178, v18, v168
	v_fmac_f32_e32 v178, v19, v166
	v_fmac_f32_e32 v178, v20, v161
	v_fmac_f32_e32 v178, v21, v162
	v_fmac_f32_e32 v178, v22, v163
	v_fmac_f32_e32 v178, v23, v164
	v_fmac_f32_e32 v178, v152, v165
	v_fmac_f32_e32 v178, v154, v167
	v_fmac_f32_e32 v178, v155, v174
	v_fmac_f32_e32 v178, v156, v176
	v_fmac_f32_e32 v178, v157, v177
	v_fmac_f32_e32 v178, v158, v192
	v_fmac_f32_e32 v178, v159, v193
	ds_write_b32 v89, v178
	ds_read_u16 v178, v35 offset:45056
	s_waitcnt lgkmcnt(0)
	v_lshlrev_b32_e32 v194, 16, v178
	v_fma_f32 v178, v0, v196, v160
	v_fmac_f32_e32 v178, v1, v198
	v_fmac_f32_e32 v178, v2, v205
	v_fmac_f32_e32 v178, v3, v204
	v_fmac_f32_e32 v178, v4, v203
	v_fmac_f32_e32 v178, v5, v202
	v_fmac_f32_e32 v178, v6, v201
	v_fmac_f32_e32 v178, v7, v200
	v_fmac_f32_e32 v178, v8, v199
	v_fmac_f32_e32 v178, v9, v197
	v_fmac_f32_e32 v178, v10, v195
	v_fmac_f32_e32 v178, v11, v175
	v_fmac_f32_e32 v178, v12, v173
	v_fmac_f32_e32 v178, v13, v172
	v_fmac_f32_e32 v178, v14, v171
	v_fmac_f32_e32 v178, v15, v170
	v_fmac_f32_e32 v178, v16, v169
	v_fmac_f32_e32 v178, v17, v168
	v_fmac_f32_e32 v178, v18, v166
	v_fmac_f32_e32 v178, v19, v161
	v_fmac_f32_e32 v178, v20, v162
	v_fmac_f32_e32 v178, v21, v163
	v_fmac_f32_e32 v178, v22, v164
	v_fmac_f32_e32 v178, v23, v165
	v_fmac_f32_e32 v178, v152, v167
	v_fmac_f32_e32 v178, v154, v174
	v_fmac_f32_e32 v178, v155, v176
	v_fmac_f32_e32 v178, v156, v177
	v_fmac_f32_e32 v178, v157, v192
	v_fmac_f32_e32 v178, v158, v193
	v_fmac_f32_e32 v178, v159, v194
	ds_write_b32 v90, v178
	ds_read_u16 v178, v35 offset:46080
	s_waitcnt lgkmcnt(0)
; __device__ __forceinline__ void phase_even_mix(CArgs a, LAS unsigned char* lds, int i2, int wv, int xw  ) {
;     ...
;             for (int r = 0; r < 64; ++r) {
;                 win[r % 34] = bf2f(glu[r * 512 + c]);
;                 if (r >= 32) { float y = cb;
; #pragma unroll
;                     for (int k = 0; k < 31; ++k) y += w[k] * win[(r - 30 + k) % 34];
;                     ybuf[(r - 32) * 512 + c] = y; }
	v_lshlrev_b32_e32 v196, 16, v178
	v_fma_f32 v178, v0, v198, v160
	v_fmac_f32_e32 v178, v1, v205
	v_fmac_f32_e32 v178, v2, v204
	v_fmac_f32_e32 v178, v3, v203
	v_fmac_f32_e32 v178, v4, v202
	v_fmac_f32_e32 v178, v5, v201
	v_fmac_f32_e32 v178, v6, v200
	v_fmac_f32_e32 v178, v7, v199
	v_fmac_f32_e32 v178, v8, v197
	v_fmac_f32_e32 v178, v9, v195
	v_fmac_f32_e32 v178, v10, v175
	v_fmac_f32_e32 v178, v11, v173
	v_fmac_f32_e32 v178, v12, v172
	v_fmac_f32_e32 v178, v13, v171
	v_fmac_f32_e32 v178, v14, v170
	v_fmac_f32_e32 v178, v15, v169
	v_fmac_f32_e32 v178, v16, v168
	v_fmac_f32_e32 v178, v17, v166
	v_fmac_f32_e32 v178, v18, v161
	v_fmac_f32_e32 v178, v19, v162
	v_fmac_f32_e32 v178, v20, v163
	v_fmac_f32_e32 v178, v21, v164
	v_fmac_f32_e32 v178, v22, v165
	v_fmac_f32_e32 v178, v23, v167
	v_fmac_f32_e32 v178, v152, v174
	v_fmac_f32_e32 v178, v154, v176
	v_fmac_f32_e32 v178, v155, v177
	v_fmac_f32_e32 v178, v156, v192
	v_fmac_f32_e32 v178, v157, v193
	v_fmac_f32_e32 v178, v158, v194
	v_fmac_f32_e32 v178, v159, v196
	ds_write_b32 v91, v178
	ds_read_u16 v178, v35 offset:47104
	s_waitcnt lgkmcnt(0)
	v_lshlrev_b32_e32 v198, 16, v178
	v_fma_f32 v178, v0, v205, v160
	v_fmac_f32_e32 v178, v1, v204
	v_fmac_f32_e32 v178, v2, v203
	v_fmac_f32_e32 v178, v3, v202
	v_fmac_f32_e32 v178, v4, v201
	v_fmac_f32_e32 v178, v5, v200
	v_fmac_f32_e32 v178, v6, v199
	v_fmac_f32_e32 v178, v7, v197
	v_fmac_f32_e32 v178, v8, v195
	v_fmac_f32_e32 v178, v9, v175
	v_fmac_f32_e32 v178, v10, v173
	v_fmac_f32_e32 v178, v11, v172
	v_fmac_f32_e32 v178, v12, v171
	v_fmac_f32_e32 v178, v13, v170
	v_fmac_f32_e32 v178, v14, v169
	v_fmac_f32_e32 v178, v15, v168
	v_fmac_f32_e32 v178, v16, v166
	v_fmac_f32_e32 v178, v17, v161
	v_fmac_f32_e32 v178, v18, v162
	v_fmac_f32_e32 v178, v19, v163
	v_fmac_f32_e32 v178, v20, v164
	v_fmac_f32_e32 v178, v21, v165
	v_fmac_f32_e32 v178, v22, v167
	v_fmac_f32_e32 v178, v23, v174
	v_fmac_f32_e32 v178, v152, v176
	v_fmac_f32_e32 v178, v154, v177
	v_fmac_f32_e32 v178, v155, v192
	v_fmac_f32_e32 v178, v156, v193
	v_fmac_f32_e32 v178, v157, v194
	v_fmac_f32_e32 v178, v158, v196
	v_fmac_f32_e32 v178, v159, v198
	ds_write_b32 v92, v178
	v_fma_f32 v178, v0, v204, v160
	v_fmac_f32_e32 v178, v1, v203
	v_fmac_f32_e32 v178, v2, v202
	v_fmac_f32_e32 v178, v3, v201
	v_fmac_f32_e32 v178, v4, v200
	v_fmac_f32_e32 v178, v5, v199
	v_fmac_f32_e32 v178, v6, v197
	v_fmac_f32_e32 v178, v7, v195
	v_fmac_f32_e32 v178, v8, v175
	v_fmac_f32_e32 v178, v9, v173
	v_fmac_f32_e32 v178, v10, v172
	v_fmac_f32_e32 v178, v11, v171
	v_fmac_f32_e32 v178, v12, v170
	v_fmac_f32_e32 v178, v13, v169
	v_fmac_f32_e32 v178, v14, v168
	v_fmac_f32_e32 v178, v15, v166
	v_fmac_f32_e32 v178, v16, v161
	v_fmac_f32_e32 v178, v17, v162
	v_fmac_f32_e32 v178, v18, v163
	v_fmac_f32_e32 v178, v19, v164
	v_fmac_f32_e32 v178, v20, v165
	v_fmac_f32_e32 v178, v21, v167
	v_fmac_f32_e32 v178, v22, v174
	v_fmac_f32_e32 v178, v23, v176
	ds_read_u16 v205, v35 offset:48128
	v_fmac_f32_e32 v178, v152, v177
	v_fmac_f32_e32 v178, v154, v192
	v_fmac_f32_e32 v178, v155, v193
	v_fmac_f32_e32 v178, v156, v194
	v_fmac_f32_e32 v178, v157, v196
	s_waitcnt lgkmcnt(0)
	v_lshlrev_b32_e32 v205, 16, v205
	v_fmac_f32_e32 v178, v158, v198
	v_fmac_f32_e32 v178, v159, v205
	ds_write_b32 v93, v178
	ds_read_u16 v178, v35 offset:49152
	s_waitcnt lgkmcnt(0)
	v_lshlrev_b32_e32 v204, 16, v178
	v_fma_f32 v178, v0, v203, v160
	v_fmac_f32_e32 v178, v1, v202
	v_fmac_f32_e32 v178, v2, v201
	v_fmac_f32_e32 v178, v3, v200
	v_fmac_f32_e32 v178, v4, v199
	v_fmac_f32_e32 v178, v5, v197
	v_fmac_f32_e32 v178, v6, v195
	v_fmac_f32_e32 v178, v7, v175
	v_fmac_f32_e32 v178, v8, v173
	v_fmac_f32_e32 v178, v9, v172
	v_fmac_f32_e32 v178, v10, v171
	v_fmac_f32_e32 v178, v11, v170
	v_fmac_f32_e32 v178, v12, v169
	v_fmac_f32_e32 v178, v13, v168
	v_fmac_f32_e32 v178, v14, v166
	v_fmac_f32_e32 v178, v15, v161
	v_fmac_f32_e32 v178, v16, v162
	v_fmac_f32_e32 v178, v17, v163
	v_fmac_f32_e32 v178, v18, v164
	v_fmac_f32_e32 v178, v19, v165
	v_fmac_f32_e32 v178, v20, v167
	v_fmac_f32_e32 v178, v21, v174
	v_fmac_f32_e32 v178, v22, v176
	v_fmac_f32_e32 v178, v23, v177
	v_fmac_f32_e32 v178, v152, v192
	v_fmac_f32_e32 v178, v154, v193
	v_fmac_f32_e32 v178, v155, v194
	v_fmac_f32_e32 v178, v156, v196
	v_fmac_f32_e32 v178, v157, v198
	v_fmac_f32_e32 v178, v158, v205
	v_fmac_f32_e32 v178, v159, v204
	ds_write_b32 v94, v178
	ds_read_u16 v178, v35 offset:50176
	s_waitcnt lgkmcnt(0)
	v_lshlrev_b32_e32 v203, 16, v178
	v_fma_f32 v178, v0, v202, v160
	v_fmac_f32_e32 v178, v1, v201
	v_fmac_f32_e32 v178, v2, v200
	v_fmac_f32_e32 v178, v3, v199
	v_fmac_f32_e32 v178, v4, v197
	v_fmac_f32_e32 v178, v5, v195
	v_fmac_f32_e32 v178, v6, v175
	v_fmac_f32_e32 v178, v7, v173
	v_fmac_f32_e32 v178, v8, v172
	v_fmac_f32_e32 v178, v9, v171
	v_fmac_f32_e32 v178, v10, v170
	v_fmac_f32_e32 v178, v11, v169
	v_fmac_f32_e32 v178, v12, v168
	v_fmac_f32_e32 v178, v13, v166
	v_fmac_f32_e32 v178, v14, v161
	v_fmac_f32_e32 v178, v15, v162
	v_fmac_f32_e32 v178, v16, v163
	v_fmac_f32_e32 v178, v17, v164
	v_fmac_f32_e32 v178, v18, v165
	v_fmac_f32_e32 v178, v19, v167
	v_fmac_f32_e32 v178, v20, v174
	v_fmac_f32_e32 v178, v21, v176
	v_fmac_f32_e32 v178, v22, v177
	v_fmac_f32_e32 v178, v23, v192
	v_fmac_f32_e32 v178, v152, v193
	v_fmac_f32_e32 v178, v154, v194
	v_fmac_f32_e32 v178, v155, v196
	v_fmac_f32_e32 v178, v156, v198
	v_fmac_f32_e32 v178, v157, v205
	v_fmac_f32_e32 v178, v158, v204
	v_fmac_f32_e32 v178, v159, v203
	ds_write_b32 v95, v178
	ds_read_u16 v178, v35 offset:51200
	s_waitcnt lgkmcnt(0)
; __device__ __forceinline__ void phase_even_mix(CArgs a, LAS unsigned char* lds, int i2, int wv, int xw  ) {
;     ...
;             for (int r = 0; r < 64; ++r) {
;                 win[r % 34] = bf2f(glu[r * 512 + c]);
;                 if (r >= 32) { float y = cb;
; #pragma unroll
;                     for (int k = 0; k < 31; ++k) y += w[k] * win[(r - 30 + k) % 34];
;                     ybuf[(r - 32) * 512 + c] = y; }
	v_lshlrev_b32_e32 v202, 16, v178
	v_fma_f32 v178, v0, v201, v160
	v_fmac_f32_e32 v178, v1, v200
	v_fmac_f32_e32 v178, v2, v199
	v_fmac_f32_e32 v178, v3, v197
	v_fmac_f32_e32 v178, v4, v195
	v_fmac_f32_e32 v178, v5, v175
	v_fmac_f32_e32 v178, v6, v173
	v_fmac_f32_e32 v178, v7, v172
	v_fmac_f32_e32 v178, v8, v171
	v_fmac_f32_e32 v178, v9, v170
	v_fmac_f32_e32 v178, v10, v169
	v_fmac_f32_e32 v178, v11, v168
	v_fmac_f32_e32 v178, v12, v166
	v_fmac_f32_e32 v178, v13, v161
	v_fmac_f32_e32 v178, v14, v162
	v_fmac_f32_e32 v178, v15, v163
	v_fmac_f32_e32 v178, v16, v164
	v_fmac_f32_e32 v178, v17, v165
	v_fmac_f32_e32 v178, v18, v167
	v_fmac_f32_e32 v178, v19, v174
	v_fmac_f32_e32 v178, v20, v176
	v_fmac_f32_e32 v178, v21, v177
	v_fmac_f32_e32 v178, v22, v192
	v_fmac_f32_e32 v178, v23, v193
	v_fmac_f32_e32 v178, v152, v194
	v_fmac_f32_e32 v178, v154, v196
	v_fmac_f32_e32 v178, v155, v198
	v_fmac_f32_e32 v178, v156, v205
	v_fmac_f32_e32 v178, v157, v204
	v_fmac_f32_e32 v178, v158, v203
	v_fmac_f32_e32 v178, v159, v202
	ds_write_b32 v96, v178
	ds_read_u16 v178, v35 offset:52224
	s_waitcnt lgkmcnt(0)
	v_lshlrev_b32_e32 v201, 16, v178
	v_fma_f32 v178, v0, v200, v160
	v_fmac_f32_e32 v178, v1, v199
	v_fmac_f32_e32 v178, v2, v197
	v_fmac_f32_e32 v178, v3, v195
	v_fmac_f32_e32 v178, v4, v175
	v_fmac_f32_e32 v178, v5, v173
	v_fmac_f32_e32 v178, v6, v172
	v_fmac_f32_e32 v178, v7, v171
	v_fmac_f32_e32 v178, v8, v170
	v_fmac_f32_e32 v178, v9, v169
	v_fmac_f32_e32 v178, v10, v168
	v_fmac_f32_e32 v178, v11, v166
	v_fmac_f32_e32 v178, v12, v161
	v_fmac_f32_e32 v178, v13, v162
	v_fmac_f32_e32 v178, v14, v163
	v_fmac_f32_e32 v178, v15, v164
	v_fmac_f32_e32 v178, v16, v165
	v_fmac_f32_e32 v178, v17, v167
	v_fmac_f32_e32 v178, v18, v174
	v_fmac_f32_e32 v178, v19, v176
	v_fmac_f32_e32 v178, v20, v177
	v_fmac_f32_e32 v178, v21, v192
	v_fmac_f32_e32 v178, v22, v193
	v_fmac_f32_e32 v178, v23, v194
	v_fmac_f32_e32 v178, v152, v196
	v_fmac_f32_e32 v178, v154, v198
	v_fmac_f32_e32 v178, v155, v205
	v_fmac_f32_e32 v178, v156, v204
	v_fmac_f32_e32 v178, v157, v203
	v_fmac_f32_e32 v178, v158, v202
	v_fmac_f32_e32 v178, v159, v201
	ds_write_b32 v97, v178
	ds_read_u16 v178, v35 offset:53248
	s_waitcnt lgkmcnt(0)
	v_lshlrev_b32_e32 v200, 16, v178
	v_fma_f32 v178, v0, v199, v160
	v_fmac_f32_e32 v178, v1, v197
	v_fmac_f32_e32 v178, v2, v195
	v_fmac_f32_e32 v178, v3, v175
	v_fmac_f32_e32 v178, v4, v173
	v_fmac_f32_e32 v178, v5, v172
	v_fmac_f32_e32 v178, v6, v171
	v_fmac_f32_e32 v178, v7, v170
	v_fmac_f32_e32 v178, v8, v169
	v_fmac_f32_e32 v178, v9, v168
	v_fmac_f32_e32 v178, v10, v166
	v_fmac_f32_e32 v178, v11, v161
	v_fmac_f32_e32 v178, v12, v162
	v_fmac_f32_e32 v178, v13, v163
	v_fmac_f32_e32 v178, v14, v164
	v_fmac_f32_e32 v178, v15, v165
	v_fmac_f32_e32 v178, v16, v167
	v_fmac_f32_e32 v178, v17, v174
	v_fmac_f32_e32 v178, v18, v176
	v_fmac_f32_e32 v178, v19, v177
	v_fmac_f32_e32 v178, v20, v192
	v_fmac_f32_e32 v178, v21, v193
	v_fmac_f32_e32 v178, v22, v194
	v_fmac_f32_e32 v178, v23, v196
	v_fmac_f32_e32 v178, v152, v198
	v_fmac_f32_e32 v178, v154, v205
	v_fmac_f32_e32 v178, v155, v204
	v_fmac_f32_e32 v178, v156, v203
	v_fmac_f32_e32 v178, v157, v202
	v_fmac_f32_e32 v178, v158, v201
	v_fmac_f32_e32 v178, v159, v200
	ds_write_b32 v98, v178
	ds_read_u16 v178, v35 offset:54272
	s_waitcnt lgkmcnt(0)
	v_lshlrev_b32_e32 v199, 16, v178
	v_fma_f32 v178, v0, v197, v160
	v_fmac_f32_e32 v178, v1, v195
	v_fmac_f32_e32 v178, v2, v175
	v_fmac_f32_e32 v178, v3, v173
	v_fmac_f32_e32 v178, v4, v172
	v_fmac_f32_e32 v178, v5, v171
	v_fmac_f32_e32 v178, v6, v170
	v_fmac_f32_e32 v178, v7, v169
	v_fmac_f32_e32 v178, v8, v168
	v_fmac_f32_e32 v178, v9, v166
	v_fmac_f32_e32 v178, v10, v161
	v_fmac_f32_e32 v178, v11, v162
	v_fmac_f32_e32 v178, v12, v163
	v_fmac_f32_e32 v178, v13, v164
	v_fmac_f32_e32 v178, v14, v165
	v_fmac_f32_e32 v178, v15, v167
	v_fmac_f32_e32 v178, v16, v174
	v_fmac_f32_e32 v178, v17, v176
	v_fmac_f32_e32 v178, v18, v177
	v_fmac_f32_e32 v178, v19, v192
	v_fmac_f32_e32 v178, v20, v193
	v_fmac_f32_e32 v178, v21, v194
	v_fmac_f32_e32 v178, v22, v196
	v_fmac_f32_e32 v178, v23, v198
	v_fmac_f32_e32 v178, v152, v205
	v_fmac_f32_e32 v178, v154, v204
	v_fmac_f32_e32 v178, v155, v203
	v_fmac_f32_e32 v178, v156, v202
	v_fmac_f32_e32 v178, v157, v201
	v_fmac_f32_e32 v178, v158, v200
	v_fmac_f32_e32 v178, v159, v199
	ds_write_b32 v99, v178
	ds_read_u16 v178, v35 offset:55296
	s_waitcnt lgkmcnt(0)
; __device__ __forceinline__ void phase_even_mix(CArgs a, LAS unsigned char* lds, int i2, int wv, int xw  ) {
;     ...
;             for (int r = 0; r < 64; ++r) {
;                 win[r % 34] = bf2f(glu[r * 512 + c]);
;                 if (r >= 32) { float y = cb;
; #pragma unroll
;                     for (int k = 0; k < 31; ++k) y += w[k] * win[(r - 30 + k) % 34];
;                     ybuf[(r - 32) * 512 + c] = y; }
	v_lshlrev_b32_e32 v197, 16, v178
	v_fma_f32 v178, v0, v195, v160
	v_fmac_f32_e32 v178, v1, v175
	v_fma_f32 v175, v0, v175, v160
	v_fmac_f32_e32 v175, v1, v173
	v_fmac_f32_e32 v175, v2, v172
	v_fmac_f32_e32 v175, v3, v171
	v_fmac_f32_e32 v175, v4, v170
	v_fmac_f32_e32 v175, v5, v169
	v_fmac_f32_e32 v175, v6, v168
	v_fmac_f32_e32 v178, v2, v173
	v_fmac_f32_e32 v175, v7, v166
	v_fma_f32 v173, v0, v173, v160
	v_fmac_f32_e32 v175, v8, v161
	v_fmac_f32_e32 v173, v1, v172
	v_fmac_f32_e32 v175, v9, v162
	v_fmac_f32_e32 v173, v2, v171
	v_fmac_f32_e32 v175, v10, v163
	v_fmac_f32_e32 v173, v3, v170
	v_fmac_f32_e32 v175, v11, v164
	v_fmac_f32_e32 v173, v4, v169
	v_fmac_f32_e32 v175, v12, v165
	v_fmac_f32_e32 v173, v5, v168
	v_fmac_f32_e32 v175, v13, v167
	v_fmac_f32_e32 v173, v6, v166
	v_fmac_f32_e32 v178, v3, v172
	v_fmac_f32_e32 v175, v14, v174
	v_fmac_f32_e32 v173, v7, v161
	v_fma_f32 v172, v0, v172, v160
	v_fmac_f32_e32 v175, v15, v176
	v_fmac_f32_e32 v173, v8, v162
	v_fmac_f32_e32 v172, v1, v171
	v_fmac_f32_e32 v175, v16, v177
	v_fmac_f32_e32 v173, v9, v163
	v_fmac_f32_e32 v172, v2, v170
	v_fmac_f32_e32 v175, v17, v192
	v_fmac_f32_e32 v173, v10, v164
	v_fmac_f32_e32 v172, v3, v169
	v_fmac_f32_e32 v175, v18, v193
	v_fmac_f32_e32 v173, v11, v165
	v_fmac_f32_e32 v172, v4, v168
	v_fmac_f32_e32 v175, v19, v194
	v_fmac_f32_e32 v173, v12, v167
	v_fmac_f32_e32 v172, v5, v166
	v_fmac_f32_e32 v175, v20, v196
	v_fmac_f32_e32 v173, v13, v174
	v_fmac_f32_e32 v172, v6, v161
	v_fmac_f32_e32 v178, v4, v171
	v_fmac_f32_e32 v175, v21, v198
	v_fmac_f32_e32 v173, v14, v176
	v_fmac_f32_e32 v172, v7, v162
	v_fma_f32 v171, v0, v171, v160
	v_fmac_f32_e32 v175, v22, v205
	v_fmac_f32_e32 v173, v15, v177
	v_fmac_f32_e32 v172, v8, v163
	v_fmac_f32_e32 v171, v1, v170
	v_fmac_f32_e32 v175, v23, v204
	v_fmac_f32_e32 v173, v16, v192
	v_fmac_f32_e32 v172, v9, v164
	v_fmac_f32_e32 v171, v2, v169
	ds_read_u16 v195, v35 offset:56320
	v_fmac_f32_e32 v175, v152, v203
	v_fmac_f32_e32 v173, v17, v193
	v_fmac_f32_e32 v172, v10, v165
	v_fmac_f32_e32 v171, v3, v168
	v_fmac_f32_e32 v175, v154, v202
	v_fmac_f32_e32 v173, v18, v194
	v_fmac_f32_e32 v172, v11, v167
	v_fmac_f32_e32 v171, v4, v166
	v_fmac_f32_e32 v175, v155, v201
	v_fmac_f32_e32 v173, v19, v196
	v_fmac_f32_e32 v172, v12, v174
	v_fmac_f32_e32 v171, v5, v161
	v_fmac_f32_e32 v175, v156, v200
	v_fmac_f32_e32 v173, v20, v198
	v_fmac_f32_e32 v172, v13, v176
	v_fmac_f32_e32 v171, v6, v162
	v_fmac_f32_e32 v178, v5, v170
	v_fmac_f32_e32 v175, v157, v199
	v_fmac_f32_e32 v173, v21, v205
	v_fmac_f32_e32 v172, v14, v177
	v_fmac_f32_e32 v171, v7, v163
	v_fma_f32 v170, v0, v170, v160
	s_waitcnt lgkmcnt(0)
	v_lshlrev_b32_e32 v195, 16, v195
	v_fmac_f32_e32 v175, v158, v197
	v_fmac_f32_e32 v173, v22, v204
	v_fmac_f32_e32 v172, v15, v192
	v_fmac_f32_e32 v171, v8, v164
	v_fmac_f32_e32 v170, v1, v169
	v_fmac_f32_e32 v175, v159, v195
	v_fmac_f32_e32 v173, v23, v203
	v_fmac_f32_e32 v172, v16, v193
	v_fmac_f32_e32 v171, v9, v165
	v_fmac_f32_e32 v170, v2, v168
	ds_write_b32 v101, v175
	ds_read_u16 v175, v35 offset:57344
	v_fmac_f32_e32 v173, v152, v202
	v_fmac_f32_e32 v172, v17, v194
	v_fmac_f32_e32 v171, v10, v167
	v_fmac_f32_e32 v170, v3, v166
	v_fmac_f32_e32 v173, v154, v201
	v_fmac_f32_e32 v172, v18, v196
	v_fmac_f32_e32 v171, v11, v174
	v_fmac_f32_e32 v170, v4, v161
	v_fmac_f32_e32 v173, v155, v200
	v_fmac_f32_e32 v172, v19, v198
	v_fmac_f32_e32 v171, v12, v176
	v_fmac_f32_e32 v170, v5, v162
	v_fmac_f32_e32 v173, v156, v199
	v_fmac_f32_e32 v172, v20, v205
	v_fmac_f32_e32 v171, v13, v177
	v_fmac_f32_e32 v170, v6, v163
	v_fmac_f32_e32 v178, v6, v169
	v_fmac_f32_e32 v173, v157, v197
	v_fmac_f32_e32 v172, v21, v204
	v_fmac_f32_e32 v171, v14, v192
	v_fmac_f32_e32 v170, v7, v164
	v_fma_f32 v169, v0, v169, v160
	s_waitcnt lgkmcnt(0)
	v_lshlrev_b32_e32 v175, 16, v175
	v_fmac_f32_e32 v173, v158, v195
	v_fmac_f32_e32 v172, v22, v203
	v_fmac_f32_e32 v171, v15, v193
	v_fmac_f32_e32 v170, v8, v165
	v_fmac_f32_e32 v169, v1, v168
	v_fmac_f32_e32 v173, v159, v175
	v_fmac_f32_e32 v172, v23, v202
	v_fmac_f32_e32 v171, v16, v194
	v_fmac_f32_e32 v170, v9, v167
	v_fmac_f32_e32 v169, v2, v166
	ds_write_b32 v102, v173
	ds_read_u16 v173, v35 offset:58368
	v_fmac_f32_e32 v172, v152, v201
	v_fmac_f32_e32 v171, v17, v196
	v_fmac_f32_e32 v170, v10, v174
	v_fmac_f32_e32 v169, v3, v161
	v_fmac_f32_e32 v172, v154, v200
	v_fmac_f32_e32 v171, v18, v198
	v_fmac_f32_e32 v170, v11, v176
	v_fmac_f32_e32 v169, v4, v162
	v_fmac_f32_e32 v172, v155, v199
	v_fmac_f32_e32 v171, v19, v205
	v_fmac_f32_e32 v170, v12, v177
	v_fmac_f32_e32 v169, v5, v163
	v_fmac_f32_e32 v172, v156, v197
	v_fmac_f32_e32 v171, v20, v204
	v_fmac_f32_e32 v170, v13, v192
	v_fmac_f32_e32 v169, v6, v164
	v_fmac_f32_e32 v178, v7, v168
	v_fmac_f32_e32 v172, v157, v195
	v_fmac_f32_e32 v171, v21, v203
	v_fmac_f32_e32 v170, v14, v193
	v_fmac_f32_e32 v169, v7, v165
	v_fma_f32 v168, v0, v168, v160
	s_waitcnt lgkmcnt(0)
	v_lshlrev_b32_e32 v173, 16, v173
	v_fmac_f32_e32 v172, v158, v175
	v_fmac_f32_e32 v171, v22, v202
	v_fmac_f32_e32 v170, v15, v194
	v_fmac_f32_e32 v169, v8, v167
	v_fmac_f32_e32 v168, v1, v166
	v_fmac_f32_e32 v172, v159, v173
	v_fmac_f32_e32 v171, v23, v201
	v_fmac_f32_e32 v170, v16, v196
	v_fmac_f32_e32 v169, v9, v174
	v_fmac_f32_e32 v168, v2, v161
	ds_write_b32 v103, v172
	ds_read_u16 v172, v35 offset:59392
	v_fmac_f32_e32 v171, v152, v200
	v_fmac_f32_e32 v170, v17, v198
	v_fmac_f32_e32 v169, v10, v176
	v_fmac_f32_e32 v168, v3, v162
	v_fmac_f32_e32 v171, v154, v199
	v_fmac_f32_e32 v170, v18, v205
	v_fmac_f32_e32 v169, v11, v177
	v_fmac_f32_e32 v168, v4, v163
	v_fmac_f32_e32 v171, v155, v197
	v_fmac_f32_e32 v170, v19, v204
	v_fmac_f32_e32 v169, v12, v192
	v_fmac_f32_e32 v168, v5, v164
	v_fmac_f32_e32 v171, v156, v195
	v_fmac_f32_e32 v170, v20, v203
	v_fmac_f32_e32 v169, v13, v193
	v_fmac_f32_e32 v168, v6, v165
	v_fmac_f32_e32 v178, v8, v166
	v_fmac_f32_e32 v171, v157, v175
	v_fmac_f32_e32 v170, v21, v202
	v_fmac_f32_e32 v169, v14, v194
	v_fmac_f32_e32 v168, v7, v167
	v_fma_f32 v166, v0, v166, v160
	s_waitcnt lgkmcnt(0)
; __device__ __forceinline__ void phase_even_mix(CArgs a, LAS unsigned char* lds, int i2, int wv, int xw  ) {
;     ...
;             for (int r = 0; r < 64; ++r) {
;                 win[r % 34] = bf2f(glu[r * 512 + c]);
;                 if (r >= 32) { float y = cb;
; #pragma unroll
;                     for (int k = 0; k < 31; ++k) y += w[k] * win[(r - 30 + k) % 34];
;                     ybuf[(r - 32) * 512 + c] = y; }
;             }
;         }
;         __syncthreads();
	v_lshlrev_b32_e32 v172, 16, v172
	v_fmac_f32_e32 v171, v158, v173
	v_fmac_f32_e32 v170, v22, v201
	v_fmac_f32_e32 v169, v15, v196
	v_fmac_f32_e32 v168, v8, v174
	v_fmac_f32_e32 v166, v1, v161
	v_fmac_f32_e32 v171, v159, v172
	v_fmac_f32_e32 v170, v23, v200
	v_fmac_f32_e32 v169, v16, v198
	v_fmac_f32_e32 v168, v9, v176
	v_fmac_f32_e32 v166, v2, v162
	ds_write_b32 v104, v171
	ds_read_u16 v171, v35 offset:60416
	v_fmac_f32_e32 v170, v152, v199
	v_fmac_f32_e32 v169, v17, v205
	v_fmac_f32_e32 v168, v10, v177
	v_fmac_f32_e32 v166, v3, v163
	v_fmac_f32_e32 v170, v154, v197
	v_fmac_f32_e32 v169, v18, v204
	v_fmac_f32_e32 v168, v11, v192
	v_fmac_f32_e32 v166, v4, v164
	v_fmac_f32_e32 v170, v155, v195
	v_fmac_f32_e32 v169, v19, v203
	v_fmac_f32_e32 v168, v12, v193
	v_fmac_f32_e32 v166, v5, v165
	v_fmac_f32_e32 v170, v156, v175
	v_fmac_f32_e32 v169, v20, v202
	v_fmac_f32_e32 v168, v13, v194
	v_fmac_f32_e32 v166, v6, v167
	v_fmac_f32_e32 v170, v157, v173
	v_fmac_f32_e32 v169, v21, v201
	v_fmac_f32_e32 v168, v14, v196
	v_fmac_f32_e32 v166, v7, v174
	v_fmac_f32_e32 v160, v0, v161
	s_waitcnt lgkmcnt(0)
	v_lshlrev_b32_e32 v171, 16, v171
	v_fmac_f32_e32 v170, v158, v172
	v_fmac_f32_e32 v169, v22, v200
	v_fmac_f32_e32 v168, v15, v198
	v_fmac_f32_e32 v166, v8, v176
	v_fmac_f32_e32 v160, v1, v162
	v_fmac_f32_e32 v170, v159, v171
	v_fmac_f32_e32 v169, v23, v199
	v_fmac_f32_e32 v168, v16, v205
	v_fmac_f32_e32 v166, v9, v177
	v_fmac_f32_e32 v160, v2, v163
	ds_write_b32 v105, v170
	ds_read_u16 v170, v35 offset:61440
	v_fmac_f32_e32 v169, v152, v197
	v_fmac_f32_e32 v168, v17, v204
	v_fmac_f32_e32 v166, v10, v192
	v_fmac_f32_e32 v160, v3, v164
	v_fmac_f32_e32 v169, v154, v195
	v_fmac_f32_e32 v168, v18, v203
	v_fmac_f32_e32 v166, v11, v193
	v_fmac_f32_e32 v160, v4, v165
	v_fmac_f32_e32 v169, v155, v175
	v_fmac_f32_e32 v168, v19, v202
	v_fmac_f32_e32 v166, v12, v194
	v_fmac_f32_e32 v160, v5, v167
	v_fmac_f32_e32 v169, v156, v173
	v_fmac_f32_e32 v168, v20, v201
	v_fmac_f32_e32 v166, v13, v196
	v_fmac_f32_e32 v160, v6, v174
	v_fmac_f32_e32 v169, v157, v172
	v_fmac_f32_e32 v168, v21, v200
	v_fmac_f32_e32 v166, v14, v198
	v_fmac_f32_e32 v160, v7, v176
	s_waitcnt lgkmcnt(0)
	v_lshlrev_b32_e32 v170, 16, v170
	v_fmac_f32_e32 v169, v158, v171
	v_fmac_f32_e32 v168, v22, v199
	v_fmac_f32_e32 v166, v15, v205
	v_fmac_f32_e32 v160, v8, v177
	v_fmac_f32_e32 v178, v9, v161
	v_fmac_f32_e32 v169, v159, v170
	v_fmac_f32_e32 v168, v23, v197
	v_fmac_f32_e32 v166, v16, v204
	v_fmac_f32_e32 v160, v9, v192
	v_fmac_f32_e32 v178, v10, v162
	ds_write_b32 v106, v169
	ds_read_u16 v169, v35 offset:62464
	v_fmac_f32_e32 v168, v152, v195
	v_fmac_f32_e32 v166, v17, v203
	v_fmac_f32_e32 v160, v10, v193
	v_fmac_f32_e32 v178, v11, v163
	v_fmac_f32_e32 v168, v154, v175
	v_fmac_f32_e32 v166, v18, v202
	v_fmac_f32_e32 v160, v11, v194
	v_fmac_f32_e32 v178, v12, v164
	v_fmac_f32_e32 v168, v155, v173
	v_fmac_f32_e32 v166, v19, v201
	v_fmac_f32_e32 v160, v12, v196
	v_fmac_f32_e32 v178, v13, v165
	v_fmac_f32_e32 v168, v156, v172
	v_fmac_f32_e32 v166, v20, v200
	v_fmac_f32_e32 v160, v13, v198
	v_fmac_f32_e32 v178, v14, v167
	v_fmac_f32_e32 v168, v157, v171
	v_fmac_f32_e32 v166, v21, v199
	v_fmac_f32_e32 v160, v14, v205
	v_fmac_f32_e32 v178, v15, v174
	s_waitcnt lgkmcnt(0)
	v_lshlrev_b32_e32 v169, 16, v169
	v_fmac_f32_e32 v168, v158, v170
	v_fmac_f32_e32 v166, v22, v197
	v_fmac_f32_e32 v160, v15, v204
	v_fmac_f32_e32 v178, v16, v176
	v_fmac_f32_e32 v168, v159, v169
	v_fmac_f32_e32 v166, v23, v195
	v_fmac_f32_e32 v160, v16, v203
	v_fmac_f32_e32 v178, v17, v177
	ds_write_b32 v107, v168
	ds_read_u16 v168, v35 offset:63488
	v_fmac_f32_e32 v166, v152, v175
	v_fmac_f32_e32 v160, v17, v202
	v_fmac_f32_e32 v178, v18, v192
	v_fmac_f32_e32 v166, v154, v173
	v_fmac_f32_e32 v160, v18, v201
	v_fmac_f32_e32 v178, v19, v193
	v_fmac_f32_e32 v166, v155, v172
	v_fmac_f32_e32 v160, v19, v200
	v_fmac_f32_e32 v178, v20, v194
	v_fmac_f32_e32 v166, v156, v171
	v_fmac_f32_e32 v160, v20, v199
	v_fmac_f32_e32 v178, v21, v196
	v_fmac_f32_e32 v166, v157, v170
	v_fmac_f32_e32 v160, v21, v197
	v_fmac_f32_e32 v178, v22, v198
	s_waitcnt lgkmcnt(0)
	v_lshlrev_b32_e32 v168, 16, v168
	v_fmac_f32_e32 v166, v158, v169
	v_fmac_f32_e32 v160, v22, v195
	v_fmac_f32_e32 v178, v23, v205
	v_fmac_f32_e32 v166, v159, v168
	v_fmac_f32_e32 v160, v23, v175
	v_fmac_f32_e32 v178, v152, v204
	ds_write_b32 v108, v166
	ds_read_u16 v166, v35 offset:64512
	v_fmac_f32_e32 v160, v152, v173
	v_fmac_f32_e32 v178, v154, v203
	v_fmac_f32_e32 v160, v154, v172
	v_fmac_f32_e32 v178, v155, v202
	v_fmac_f32_e32 v160, v155, v171
	v_fmac_f32_e32 v178, v156, v201
	v_fmac_f32_e32 v160, v156, v170
	v_fmac_f32_e32 v178, v157, v200
	v_fmac_f32_e32 v160, v157, v169
	v_fmac_f32_e32 v178, v158, v199
	s_waitcnt lgkmcnt(0)
	v_lshlrev_b32_e32 v166, 16, v166
	v_fmac_f32_e32 v160, v158, v168
	v_add_u32_e32 v152, s19, v69
	v_fmac_f32_e32 v178, v159, v197
	v_fmac_f32_e32 v160, v159, v166
	v_cmp_lt_i32_e32 vcc, -1, v152
	v_mov_b32_e32 v0, 0
	v_mov_b32_e32 v2, 0
	v_mov_b32_e32 v3, 0
	v_mov_b32_e32 v4, 0
	v_mov_b32_e32 v5, 0
	ds_write_b32 v100, v178
	ds_write_b32 v109, v160
	s_waitcnt lgkmcnt(0)
	s_barrier
; #define LAS __attribute__((address_space(3)))
; __device__ __forceinline__ void phase_even_mix(CArgs a, LAS unsigned char* lds, int i2, int wv, int xw  ) {
;     ...
;         for (int it = 0; it < 6; ++it) { const int item = it * NTHR + tid, tt = item >> 6, cg = item & 63, p = t0 - 16 + tt;
;             u32x4 o = (u32x4){0u, 0u, 0u, 0u};
;             if (p >= 0) o = *(const u32x4*)(HB + ((size_t)b * SEQ + p) * EVEN_IN + cg * 8);
;             *(LAS u32x4*)(glu + tt * 512 + cg * 8) = o; }
	v_add_u32_e32 v152, s19, v69
	v_mov_b32_e32 v200, 0
	v_cmp_lt_i32_e32 vcc, -1, v152
	v_mov_b32_e32 v201, 0
	v_mov_b32_e32 v202, 0
	v_mov_b32_e32 v203, 0
	s_nop 0
	s_and_saveexec_b64 s[16:17], vcc
	v_lshl_add_u64 v[0:1], s[92:93], 0, v[152:153]
	v_mad_u64_u32 v[2:3], s[22:23], v0, s53, v[24:25]
	v_mad_i32_i24 v3, v1, s53, v3
	global_load_dwordx4 v[200:203], v[2:3], off
	s_or_b64 exec, exec, s[16:17]
	v_add_u32_e32 v152, s19, v70
	v_mov_b32_e32 v204, 0
	v_cmp_lt_i32_e32 vcc, -1, v152
	v_mov_b32_e32 v205, 0
	v_mov_b32_e32 v206, 0
	v_mov_b32_e32 v207, 0
	s_nop 0
	s_and_saveexec_b64 s[16:17], vcc
	v_lshl_add_u64 v[0:1], s[92:93], 0, v[152:153]
	v_mad_u64_u32 v[2:3], s[22:23], v0, s53, v[24:25]
	v_mad_i32_i24 v3, v1, s53, v3
	global_load_dwordx4 v[204:207], v[2:3], off
	s_or_b64 exec, exec, s[16:17]
	v_add_u32_e32 v152, s19, v71
	v_mov_b32_e32 v208, 0
	v_cmp_lt_i32_e32 vcc, -1, v152
	v_mov_b32_e32 v209, 0
	v_mov_b32_e32 v210, 0
	v_mov_b32_e32 v211, 0
	s_nop 0
	s_and_saveexec_b64 s[16:17], vcc
	v_lshl_add_u64 v[0:1], s[92:93], 0, v[152:153]
	v_mad_u64_u32 v[2:3], s[22:23], v0, s53, v[24:25]
	v_mad_i32_i24 v3, v1, s53, v3
	global_load_dwordx4 v[208:211], v[2:3], off
	s_or_b64 exec, exec, s[16:17]
	v_add_u32_e32 v152, s19, v72
	v_mov_b32_e32 v212, 0
	v_cmp_lt_i32_e32 vcc, -1, v152
	v_mov_b32_e32 v213, 0
	v_mov_b32_e32 v214, 0
	v_mov_b32_e32 v215, 0
	s_nop 0
	s_and_saveexec_b64 s[16:17], vcc
	v_lshl_add_u64 v[0:1], s[92:93], 0, v[152:153]
	v_mad_u64_u32 v[2:3], s[22:23], v0, s53, v[24:25]
	v_mad_i32_i24 v3, v1, s53, v3
	global_load_dwordx4 v[212:215], v[2:3], off
	s_or_b64 exec, exec, s[16:17]
	v_add_u32_e32 v152, s19, v73
	v_mov_b32_e32 v216, 0
	v_cmp_lt_i32_e32 vcc, -1, v152
	v_mov_b32_e32 v217, 0
	v_mov_b32_e32 v218, 0
	v_mov_b32_e32 v219, 0
	s_nop 0
	s_and_saveexec_b64 s[16:17], vcc
	v_lshl_add_u64 v[0:1], s[92:93], 0, v[152:153]
	v_mad_u64_u32 v[2:3], s[22:23], v0, s53, v[24:25]
	v_mad_i32_i24 v3, v1, s53, v3
	global_load_dwordx4 v[216:219], v[2:3], off
	s_or_b64 exec, exec, s[16:17]
	v_add_u32_e32 v152, s19, v74
	v_mov_b32_e32 v220, 0
	v_cmp_lt_i32_e32 vcc, -1, v152
	v_mov_b32_e32 v221, 0
	v_mov_b32_e32 v222, 0
	v_mov_b32_e32 v223, 0
	s_nop 0
	s_and_saveexec_b64 s[16:17], vcc
	v_lshl_add_u64 v[0:1], s[92:93], 0, v[152:153]
	v_mad_u64_u32 v[2:3], s[22:23], v0, s53, v[24:25]
	v_mad_i32_i24 v3, v1, s53, v3
	global_load_dwordx4 v[220:223], v[2:3], off
	s_or_b64 exec, exec, s[16:17]
	s_waitcnt vmcnt(5)
	ds_write_b128 v146, v[200:203]
	s_waitcnt vmcnt(4)
	ds_write_b128 v147, v[204:207]
	s_waitcnt vmcnt(3)
	ds_write_b128 v148, v[208:211]
	s_waitcnt vmcnt(2)
	ds_write_b128 v149, v[212:215]
	s_waitcnt vmcnt(1)
	ds_write_b128 v150, v[216:219]
	s_waitcnt vmcnt(0)
	ds_write_b128 v151, v[220:223]
	s_branch .LBB0_460
